# K1: total-sum computed once from the column accumulators instead of per iteration (16 fewer VALU per wave)
# speedup vs baseline: 1.0079x; 1.0026x over previous
.LBB0_8:
	s_bitcmp1_b32 s15, 8
	s_cselect_b64 s[20:21], -1, 0
	s_lshr_b32 s16, s15, 2
	s_and_b32 s16, s16, 63
	s_lshl_b64 s[4:5], 1, s16
	s_waitcnt vmcnt(12)
	v_pk_add_f32 v[72:73], v[26:27], v[28:29]
	v_pk_add_f32 v[74:75], v[10:11], v[12:13]
	v_pk_add_f32 v[76:77], v[34:35], v[36:37]
	v_pk_add_f32 v[78:79], v[14:15], v[16:17]
	v_pk_add_f32 v[58:59], v[26:27], v[34:35]
	v_pk_add_f32 v[60:61], v[28:29], v[36:37]
	v_pk_add_f32 v[72:73], v[72:73], v[74:75]
	v_pk_add_f32 v[76:77], v[76:77], v[78:79]
	v_pk_add_f32 v[54:55], v[10:11], v[14:15]
	v_pk_add_f32 v[56:57], v[12:13], v[16:17]
	v_add_f32_e32 v50, v72, v73
	v_add_f32_e32 v51, v76, v77
	s_waitcnt vmcnt(8)
	v_pk_add_f32 v[72:73], v[30:31], v[32:33]
	v_pk_add_f32 v[74:75], v[18:19], v[20:21]
	v_pk_add_f32 v[76:77], v[38:39], v[40:41]
	v_pk_add_f32 v[78:79], v[22:23], v[24:25]
	v_pk_add_f32 v[48:49], v[30:31], v[38:39]
	v_pk_add_f32 v[70:71], v[32:33], v[40:41]
	v_pk_add_f32 v[72:73], v[72:73], v[74:75]
	v_pk_add_f32 v[76:77], v[76:77], v[78:79]
	v_pk_add_f32 v[58:59], v[58:59], v[48:49]
	v_pk_add_f32 v[60:61], v[60:61], v[70:71]
	v_pk_add_f32 v[48:49], v[18:19], v[22:23]
	v_pk_add_f32 v[70:71], v[20:21], v[24:25]
	v_add_f32_e32 v52, v72, v73
	v_add_f32_e32 v53, v76, v77
	v_pk_add_f32 v[2:3], v[2:3], v[58:59]
	v_pk_add_f32 v[4:5], v[4:5], v[60:61]
	v_pk_add_f32 v[54:55], v[54:55], v[48:49]
	v_pk_add_f32 v[56:57], v[56:57], v[70:71]
	v_pk_add_f32 v[6:7], v[6:7], v[54:55]
	v_pk_add_f32 v[8:9], v[8:9], v[56:57]
	v_add_f32_dpp v50, v50, v50 quad_perm:[1,0,3,2] row_mask:0xf bank_mask:0xf
	v_add_f32_dpp v51, v51, v51 quad_perm:[1,0,3,2] row_mask:0xf bank_mask:0xf
	v_add_f32_dpp v52, v52, v52 quad_perm:[1,0,3,2] row_mask:0xf bank_mask:0xf
	v_add_f32_dpp v53, v53, v53 quad_perm:[1,0,3,2] row_mask:0xf bank_mask:0xf
	v_add_f32_dpp v50, v50, v50 quad_perm:[2,3,0,1] row_mask:0xf bank_mask:0xf
	v_add_f32_dpp v51, v51, v51 quad_perm:[2,3,0,1] row_mask:0xf bank_mask:0xf
	v_add_f32_dpp v52, v52, v52 quad_perm:[2,3,0,1] row_mask:0xf bank_mask:0xf
	v_add_f32_dpp v53, v53, v53 quad_perm:[2,3,0,1] row_mask:0xf bank_mask:0xf
	v_add_f32_dpp v50, v50, v50 row_half_mirror row_mask:0xf bank_mask:0xf
	v_add_f32_dpp v51, v51, v51 row_half_mirror row_mask:0xf bank_mask:0xf
	v_add_f32_dpp v52, v52, v52 row_half_mirror row_mask:0xf bank_mask:0xf
	v_add_f32_dpp v53, v53, v53 row_half_mirror row_mask:0xf bank_mask:0xf
	v_add_f32_dpp v50, v50, v50 row_mirror row_mask:0xf bank_mask:0xf
	v_add_f32_dpp v51, v51, v51 row_mirror row_mask:0xf bank_mask:0xf
	v_add_f32_dpp v52, v52, v52 row_mirror row_mask:0xf bank_mask:0xf
	v_add_f32_dpp v53, v53, v53 row_mirror row_mask:0xf bank_mask:0xf
	v_add_f32_dpp v50, v50, v50 row_bcast:15 row_mask:0xa bank_mask:0xf
	v_add_f32_dpp v51, v51, v51 row_bcast:15 row_mask:0xa bank_mask:0xf
	v_add_f32_dpp v52, v52, v52 row_bcast:15 row_mask:0xa bank_mask:0xf
	v_add_f32_dpp v53, v53, v53 row_bcast:15 row_mask:0xa bank_mask:0xf
	v_add_f32_dpp v50, v50, v50 row_bcast:31 row_mask:0xc bank_mask:0xf
	v_add_f32_dpp v51, v51, v51 row_bcast:31 row_mask:0xc bank_mask:0xf
	v_add_f32_dpp v52, v52, v52 row_bcast:31 row_mask:0xc bank_mask:0xf
	v_add_f32_dpp v53, v53, v53 row_bcast:31 row_mask:0xc bank_mask:0xf
	s_mov_b64 exec, s[4:5]
	v_cndmask_b32_e64 v58, v26, v10, s[20:21]
	v_cndmask_b32_e64 v59, v35, v15, s[20:21]
	v_cndmask_b32_e64 v60, v32, v20, s[20:21]
	v_cndmask_b32_e64 v61, v41, v25, s[20:21]
	global_store_dwordx4 v[44:45], v[58:61], off
	v_add_f32_e32 v72, v58, v59
	v_add_f32_e32 v73, v60, v61
	v_add_f32_e32 v72, v72, v73
	v_add_f32_e32 v42, v42, v72
	s_mov_b32 s4, 0
	s_brev_b32 s5, 1
	s_mov_b64 exec, s[4:5]
	v_lshl_add_u64 v[72:73], v[44:45], 0, s[18:19]
	global_store_dwordx4 v[72:73], v[50:53], off
	s_mov_b64 exec, -1
	s_add_u32 s15, s15, 16
	v_lshl_add_u64 v[44:45], v[44:45], 0, 64
	v_add_u32_e32 v46, 0x10000, v68
	buffer_load_dwordx4 v[26:29], v46, s[8:11], 0 offen sc0 nt
	buffer_load_dwordx4 v[10:13], v46, s[8:11], 0 offen offset:1024 sc0 nt
	buffer_load_dwordx4 v[34:37], v46, s[8:11], 0 offen offset:2048 sc0 nt
	buffer_load_dwordx4 v[14:17], v46, s[8:11], 0 offen offset:3072 sc0 nt
	v_add_u32_e32 v47, 0x1000, v46
	buffer_load_dwordx4 v[30:33], v47, s[8:11], 0 offen sc0 nt
	buffer_load_dwordx4 v[18:21], v47, s[8:11], 0 offen offset:1024 sc0 nt
	buffer_load_dwordx4 v[38:41], v47, s[8:11], 0 offen offset:2048 sc0 nt
	buffer_load_dwordx4 v[22:25], v47, s[8:11], 0 offen offset:3072 sc0 nt
	s_bitcmp1_b32 s15, 8
	s_cselect_b64 s[20:21], -1, 0
	s_lshr_b32 s16, s15, 2
	s_and_b32 s16, s16, 63
	s_lshl_b64 s[4:5], 1, s16
	s_waitcnt vmcnt(14)
	v_pk_add_f32 v[72:73], v[96:97], v[98:99]
	v_pk_add_f32 v[74:75], v[80:81], v[82:83]
	v_pk_add_f32 v[76:77], v[104:105], v[106:107]
	v_pk_add_f32 v[78:79], v[84:85], v[86:87]
	v_pk_add_f32 v[58:59], v[96:97], v[104:105]
	v_pk_add_f32 v[60:61], v[98:99], v[106:107]
	v_pk_add_f32 v[72:73], v[72:73], v[74:75]
	v_pk_add_f32 v[76:77], v[76:77], v[78:79]
	v_pk_add_f32 v[54:55], v[80:81], v[84:85]
	v_pk_add_f32 v[56:57], v[82:83], v[86:87]
	v_add_f32_e32 v50, v72, v73
	v_add_f32_e32 v51, v76, v77
	s_waitcnt vmcnt(10)
	v_pk_add_f32 v[72:73], v[100:101], v[102:103]
	v_pk_add_f32 v[74:75], v[88:89], v[90:91]
	v_pk_add_f32 v[76:77], v[108:109], v[110:111]
	v_pk_add_f32 v[78:79], v[92:93], v[94:95]
	v_pk_add_f32 v[48:49], v[100:101], v[108:109]
	v_pk_add_f32 v[70:71], v[102:103], v[110:111]
	v_pk_add_f32 v[72:73], v[72:73], v[74:75]
	v_pk_add_f32 v[76:77], v[76:77], v[78:79]
	v_pk_add_f32 v[58:59], v[58:59], v[48:49]
	v_pk_add_f32 v[60:61], v[60:61], v[70:71]
	v_pk_add_f32 v[48:49], v[88:89], v[92:93]
	v_pk_add_f32 v[70:71], v[90:91], v[94:95]
	v_add_f32_e32 v52, v72, v73
	v_add_f32_e32 v53, v76, v77
	v_pk_add_f32 v[2:3], v[2:3], v[58:59]
	v_pk_add_f32 v[4:5], v[4:5], v[60:61]
	v_pk_add_f32 v[54:55], v[54:55], v[48:49]
	v_pk_add_f32 v[56:57], v[56:57], v[70:71]
	v_pk_add_f32 v[6:7], v[6:7], v[54:55]
	v_pk_add_f32 v[8:9], v[8:9], v[56:57]
	v_add_f32_dpp v50, v50, v50 quad_perm:[1,0,3,2] row_mask:0xf bank_mask:0xf
	v_add_f32_dpp v51, v51, v51 quad_perm:[1,0,3,2] row_mask:0xf bank_mask:0xf
	v_add_f32_dpp v52, v52, v52 quad_perm:[1,0,3,2] row_mask:0xf bank_mask:0xf
	v_add_f32_dpp v53, v53, v53 quad_perm:[1,0,3,2] row_mask:0xf bank_mask:0xf
	v_add_f32_dpp v50, v50, v50 quad_perm:[2,3,0,1] row_mask:0xf bank_mask:0xf
	v_add_f32_dpp v51, v51, v51 quad_perm:[2,3,0,1] row_mask:0xf bank_mask:0xf
	v_add_f32_dpp v52, v52, v52 quad_perm:[2,3,0,1] row_mask:0xf bank_mask:0xf
	v_add_f32_dpp v53, v53, v53 quad_perm:[2,3,0,1] row_mask:0xf bank_mask:0xf
	v_add_f32_dpp v50, v50, v50 row_half_mirror row_mask:0xf bank_mask:0xf
	v_add_f32_dpp v51, v51, v51 row_half_mirror row_mask:0xf bank_mask:0xf
	v_add_f32_dpp v52, v52, v52 row_half_mirror row_mask:0xf bank_mask:0xf
	v_add_f32_dpp v53, v53, v53 row_half_mirror row_mask:0xf bank_mask:0xf
	v_add_f32_dpp v50, v50, v50 row_mirror row_mask:0xf bank_mask:0xf
	v_add_f32_dpp v51, v51, v51 row_mirror row_mask:0xf bank_mask:0xf
	v_add_f32_dpp v52, v52, v52 row_mirror row_mask:0xf bank_mask:0xf
	v_add_f32_dpp v53, v53, v53 row_mirror row_mask:0xf bank_mask:0xf
	v_add_f32_dpp v50, v50, v50 row_bcast:15 row_mask:0xa bank_mask:0xf
	v_add_f32_dpp v51, v51, v51 row_bcast:15 row_mask:0xa bank_mask:0xf
	v_add_f32_dpp v52, v52, v52 row_bcast:15 row_mask:0xa bank_mask:0xf
	v_add_f32_dpp v53, v53, v53 row_bcast:15 row_mask:0xa bank_mask:0xf
	v_add_f32_dpp v50, v50, v50 row_bcast:31 row_mask:0xc bank_mask:0xf
	v_add_f32_dpp v51, v51, v51 row_bcast:31 row_mask:0xc bank_mask:0xf
	v_add_f32_dpp v52, v52, v52 row_bcast:31 row_mask:0xc bank_mask:0xf
	v_add_f32_dpp v53, v53, v53 row_bcast:31 row_mask:0xc bank_mask:0xf
	s_mov_b64 exec, s[4:5]
	v_cndmask_b32_e64 v58, v96, v80, s[20:21]
	v_cndmask_b32_e64 v59, v105, v85, s[20:21]
	v_cndmask_b32_e64 v60, v102, v90, s[20:21]
	v_cndmask_b32_e64 v61, v111, v95, s[20:21]
	global_store_dwordx4 v[44:45], v[58:61], off
	v_add_f32_e32 v72, v58, v59
	v_add_f32_e32 v73, v60, v61
	v_add_f32_e32 v72, v72, v73
	v_add_f32_e32 v42, v42, v72
	s_mov_b32 s4, 0
	s_brev_b32 s5, 1
	s_mov_b64 exec, s[4:5]
	v_lshl_add_u64 v[72:73], v[44:45], 0, s[18:19]
	global_store_dwordx4 v[72:73], v[50:53], off
	s_mov_b64 exec, -1
	s_add_u32 s15, s15, 16
	v_lshl_add_u64 v[44:45], v[44:45], 0, 64
	v_add_u32_e32 v46, 0x18000, v68
	buffer_load_dwordx4 v[96:99], v46, s[8:11], 0 offen sc0 nt
	buffer_load_dwordx4 v[80:83], v46, s[8:11], 0 offen offset:1024 sc0 nt
	buffer_load_dwordx4 v[104:107], v46, s[8:11], 0 offen offset:2048 sc0 nt
	buffer_load_dwordx4 v[84:87], v46, s[8:11], 0 offen offset:3072 sc0 nt
	v_add_u32_e32 v47, 0x1000, v46
	buffer_load_dwordx4 v[100:103], v47, s[8:11], 0 offen sc0 nt
	buffer_load_dwordx4 v[88:91], v47, s[8:11], 0 offen offset:1024 sc0 nt
	buffer_load_dwordx4 v[108:111], v47, s[8:11], 0 offen offset:2048 sc0 nt
	buffer_load_dwordx4 v[92:95], v47, s[8:11], 0 offen offset:3072 sc0 nt
	s_bitcmp1_b32 s15, 8
	s_cselect_b64 s[20:21], -1, 0
	s_lshr_b32 s16, s15, 2
	s_and_b32 s16, s16, 63
	s_lshl_b64 s[4:5], 1, s16
	s_waitcnt vmcnt(14)
	v_pk_add_f32 v[72:73], v[26:27], v[28:29]
	v_pk_add_f32 v[74:75], v[10:11], v[12:13]
	v_pk_add_f32 v[76:77], v[34:35], v[36:37]
	v_pk_add_f32 v[78:79], v[14:15], v[16:17]
	v_pk_add_f32 v[58:59], v[26:27], v[34:35]
	v_pk_add_f32 v[60:61], v[28:29], v[36:37]
	v_pk_add_f32 v[72:73], v[72:73], v[74:75]
	v_pk_add_f32 v[76:77], v[76:77], v[78:79]
	v_pk_add_f32 v[54:55], v[10:11], v[14:15]
	v_pk_add_f32 v[56:57], v[12:13], v[16:17]
	v_add_f32_e32 v50, v72, v73
	v_add_f32_e32 v51, v76, v77
	s_waitcnt vmcnt(10)
	v_pk_add_f32 v[72:73], v[30:31], v[32:33]
	v_pk_add_f32 v[74:75], v[18:19], v[20:21]
	v_pk_add_f32 v[76:77], v[38:39], v[40:41]
	v_pk_add_f32 v[78:79], v[22:23], v[24:25]
	v_pk_add_f32 v[48:49], v[30:31], v[38:39]
	v_pk_add_f32 v[70:71], v[32:33], v[40:41]
	v_pk_add_f32 v[72:73], v[72:73], v[74:75]
	v_pk_add_f32 v[76:77], v[76:77], v[78:79]
	v_pk_add_f32 v[58:59], v[58:59], v[48:49]
	v_pk_add_f32 v[60:61], v[60:61], v[70:71]
	v_pk_add_f32 v[48:49], v[18:19], v[22:23]
	v_pk_add_f32 v[70:71], v[20:21], v[24:25]
	v_add_f32_e32 v52, v72, v73
	v_add_f32_e32 v53, v76, v77
	v_pk_add_f32 v[2:3], v[2:3], v[58:59]
	v_pk_add_f32 v[4:5], v[4:5], v[60:61]
	v_pk_add_f32 v[54:55], v[54:55], v[48:49]
	v_pk_add_f32 v[56:57], v[56:57], v[70:71]
	v_pk_add_f32 v[6:7], v[6:7], v[54:55]
	v_pk_add_f32 v[8:9], v[8:9], v[56:57]
	v_add_f32_dpp v50, v50, v50 quad_perm:[1,0,3,2] row_mask:0xf bank_mask:0xf
	v_add_f32_dpp v51, v51, v51 quad_perm:[1,0,3,2] row_mask:0xf bank_mask:0xf
	v_add_f32_dpp v52, v52, v52 quad_perm:[1,0,3,2] row_mask:0xf bank_mask:0xf
	v_add_f32_dpp v53, v53, v53 quad_perm:[1,0,3,2] row_mask:0xf bank_mask:0xf
	v_add_f32_dpp v50, v50, v50 quad_perm:[2,3,0,1] row_mask:0xf bank_mask:0xf
	v_add_f32_dpp v51, v51, v51 quad_perm:[2,3,0,1] row_mask:0xf bank_mask:0xf
	v_add_f32_dpp v52, v52, v52 quad_perm:[2,3,0,1] row_mask:0xf bank_mask:0xf
	v_add_f32_dpp v53, v53, v53 quad_perm:[2,3,0,1] row_mask:0xf bank_mask:0xf
	v_add_f32_dpp v50, v50, v50 row_half_mirror row_mask:0xf bank_mask:0xf
	v_add_f32_dpp v51, v51, v51 row_half_mirror row_mask:0xf bank_mask:0xf
	v_add_f32_dpp v52, v52, v52 row_half_mirror row_mask:0xf bank_mask:0xf
	v_add_f32_dpp v53, v53, v53 row_half_mirror row_mask:0xf bank_mask:0xf
	v_add_f32_dpp v50, v50, v50 row_mirror row_mask:0xf bank_mask:0xf
	v_add_f32_dpp v51, v51, v51 row_mirror row_mask:0xf bank_mask:0xf
	v_add_f32_dpp v52, v52, v52 row_mirror row_mask:0xf bank_mask:0xf
	v_add_f32_dpp v53, v53, v53 row_mirror row_mask:0xf bank_mask:0xf
	v_add_f32_dpp v50, v50, v50 row_bcast:15 row_mask:0xa bank_mask:0xf
	v_add_f32_dpp v51, v51, v51 row_bcast:15 row_mask:0xa bank_mask:0xf
	v_add_f32_dpp v52, v52, v52 row_bcast:15 row_mask:0xa bank_mask:0xf
	v_add_f32_dpp v53, v53, v53 row_bcast:15 row_mask:0xa bank_mask:0xf
	v_add_f32_dpp v50, v50, v50 row_bcast:31 row_mask:0xc bank_mask:0xf
	v_add_f32_dpp v51, v51, v51 row_bcast:31 row_mask:0xc bank_mask:0xf
	v_add_f32_dpp v52, v52, v52 row_bcast:31 row_mask:0xc bank_mask:0xf
	v_add_f32_dpp v53, v53, v53 row_bcast:31 row_mask:0xc bank_mask:0xf
	s_mov_b64 exec, s[4:5]
	v_cndmask_b32_e64 v58, v26, v10, s[20:21]
	v_cndmask_b32_e64 v59, v35, v15, s[20:21]
	v_cndmask_b32_e64 v60, v32, v20, s[20:21]
	v_cndmask_b32_e64 v61, v41, v25, s[20:21]
	global_store_dwordx4 v[44:45], v[58:61], off
	v_add_f32_e32 v72, v58, v59
	v_add_f32_e32 v73, v60, v61
	v_add_f32_e32 v72, v72, v73
	v_add_f32_e32 v42, v42, v72
	s_mov_b32 s4, 0
	s_brev_b32 s5, 1
	s_mov_b64 exec, s[4:5]
	v_lshl_add_u64 v[72:73], v[44:45], 0, s[18:19]
	global_store_dwordx4 v[72:73], v[50:53], off
	s_mov_b64 exec, -1
	s_add_u32 s15, s15, 16
	v_lshl_add_u64 v[44:45], v[44:45], 0, 64
	s_bitcmp1_b32 s15, 8
	s_cselect_b64 s[20:21], -1, 0
	s_lshr_b32 s16, s15, 2
	s_and_b32 s16, s16, 63
	s_lshl_b64 s[4:5], 1, s16
	s_waitcnt vmcnt(6)
	v_pk_add_f32 v[72:73], v[96:97], v[98:99]
	v_pk_add_f32 v[74:75], v[80:81], v[82:83]
	v_pk_add_f32 v[76:77], v[104:105], v[106:107]
	v_pk_add_f32 v[78:79], v[84:85], v[86:87]
	v_pk_add_f32 v[58:59], v[96:97], v[104:105]
	v_pk_add_f32 v[60:61], v[98:99], v[106:107]
	v_pk_add_f32 v[72:73], v[72:73], v[74:75]
	v_pk_add_f32 v[76:77], v[76:77], v[78:79]
	v_pk_add_f32 v[54:55], v[80:81], v[84:85]
	v_pk_add_f32 v[56:57], v[82:83], v[86:87]
	v_add_f32_e32 v50, v72, v73
	v_add_f32_e32 v51, v76, v77
	s_waitcnt vmcnt(2)
	v_pk_add_f32 v[72:73], v[100:101], v[102:103]
	v_pk_add_f32 v[74:75], v[88:89], v[90:91]
	v_pk_add_f32 v[76:77], v[108:109], v[110:111]
	v_pk_add_f32 v[78:79], v[92:93], v[94:95]
	v_pk_add_f32 v[48:49], v[100:101], v[108:109]
	v_pk_add_f32 v[70:71], v[102:103], v[110:111]
	v_pk_add_f32 v[72:73], v[72:73], v[74:75]
	v_pk_add_f32 v[76:77], v[76:77], v[78:79]
	v_pk_add_f32 v[58:59], v[58:59], v[48:49]
	v_pk_add_f32 v[60:61], v[60:61], v[70:71]
	v_pk_add_f32 v[48:49], v[88:89], v[92:93]
	v_pk_add_f32 v[70:71], v[90:91], v[94:95]
	v_add_f32_e32 v52, v72, v73
	v_add_f32_e32 v53, v76, v77
	v_pk_add_f32 v[2:3], v[2:3], v[58:59]
	v_pk_add_f32 v[4:5], v[4:5], v[60:61]
	v_pk_add_f32 v[54:55], v[54:55], v[48:49]
	v_pk_add_f32 v[56:57], v[56:57], v[70:71]
	v_pk_add_f32 v[6:7], v[6:7], v[54:55]
	v_pk_add_f32 v[8:9], v[8:9], v[56:57]
	v_add_f32_dpp v50, v50, v50 quad_perm:[1,0,3,2] row_mask:0xf bank_mask:0xf
	v_add_f32_dpp v51, v51, v51 quad_perm:[1,0,3,2] row_mask:0xf bank_mask:0xf
	v_add_f32_dpp v52, v52, v52 quad_perm:[1,0,3,2] row_mask:0xf bank_mask:0xf
	v_add_f32_dpp v53, v53, v53 quad_perm:[1,0,3,2] row_mask:0xf bank_mask:0xf
	v_add_f32_dpp v50, v50, v50 quad_perm:[2,3,0,1] row_mask:0xf bank_mask:0xf
	v_add_f32_dpp v51, v51, v51 quad_perm:[2,3,0,1] row_mask:0xf bank_mask:0xf
	v_add_f32_dpp v52, v52, v52 quad_perm:[2,3,0,1] row_mask:0xf bank_mask:0xf
	v_add_f32_dpp v53, v53, v53 quad_perm:[2,3,0,1] row_mask:0xf bank_mask:0xf
	v_add_f32_dpp v50, v50, v50 row_half_mirror row_mask:0xf bank_mask:0xf
	v_add_f32_dpp v51, v51, v51 row_half_mirror row_mask:0xf bank_mask:0xf
	v_add_f32_dpp v52, v52, v52 row_half_mirror row_mask:0xf bank_mask:0xf
	v_add_f32_dpp v53, v53, v53 row_half_mirror row_mask:0xf bank_mask:0xf
	v_add_f32_dpp v50, v50, v50 row_mirror row_mask:0xf bank_mask:0xf
	v_add_f32_dpp v51, v51, v51 row_mirror row_mask:0xf bank_mask:0xf
	v_add_f32_dpp v52, v52, v52 row_mirror row_mask:0xf bank_mask:0xf
	v_add_f32_dpp v53, v53, v53 row_mirror row_mask:0xf bank_mask:0xf
	v_add_f32_dpp v50, v50, v50 row_bcast:15 row_mask:0xa bank_mask:0xf
	v_add_f32_dpp v51, v51, v51 row_bcast:15 row_mask:0xa bank_mask:0xf
	v_add_f32_dpp v52, v52, v52 row_bcast:15 row_mask:0xa bank_mask:0xf
	v_add_f32_dpp v53, v53, v53 row_bcast:15 row_mask:0xa bank_mask:0xf
	v_add_f32_dpp v50, v50, v50 row_bcast:31 row_mask:0xc bank_mask:0xf
	v_add_f32_dpp v51, v51, v51 row_bcast:31 row_mask:0xc bank_mask:0xf
	v_add_f32_dpp v52, v52, v52 row_bcast:31 row_mask:0xc bank_mask:0xf
	v_add_f32_dpp v53, v53, v53 row_bcast:31 row_mask:0xc bank_mask:0xf
	s_mov_b64 exec, s[4:5]
	v_cndmask_b32_e64 v58, v96, v80, s[20:21]
	v_cndmask_b32_e64 v59, v105, v85, s[20:21]
	v_cndmask_b32_e64 v60, v102, v90, s[20:21]
	v_cndmask_b32_e64 v61, v111, v95, s[20:21]
	global_store_dwordx4 v[44:45], v[58:61], off
	v_add_f32_e32 v72, v58, v59
	v_add_f32_e32 v73, v60, v61
	v_add_f32_e32 v72, v72, v73
	v_add_f32_e32 v42, v42, v72
	s_mov_b32 s4, 0
	s_brev_b32 s5, 1
	s_mov_b64 exec, s[4:5]
	v_lshl_add_u64 v[72:73], v[44:45], 0, s[18:19]
	global_store_dwordx4 v[72:73], v[50:53], off
	s_mov_b64 exec, -1
	s_add_u32 s15, s15, 16
	v_lshl_add_u64 v[44:45], v[44:45], 0, 64
.LBB0_12:
.LBB0_20:
	v_lshl_or_b32 v1, v62, 11, v63
	ds_write_b128 v1, v[2:5]
	ds_write_b128 v1, v[6:9] offset:1024
	v_pk_add_f32 v[72:73], v[2:3], v[4:5]
	v_pk_add_f32 v[74:75], v[6:7], v[8:9]
	v_pk_add_f32 v[72:73], v[72:73], v[74:75]
	s_nop 0
	v_add_f32_e32 v43, v72, v73
	s_nop 1
	v_add_f32_dpp v42, v42, v42 quad_perm:[1,0,3,2] row_mask:0xf bank_mask:0xf
	v_add_f32_dpp v43, v43, v43 quad_perm:[1,0,3,2] row_mask:0xf bank_mask:0xf
	s_nop 0
	v_add_f32_dpp v42, v42, v42 quad_perm:[2,3,0,1] row_mask:0xf bank_mask:0xf
	v_add_f32_dpp v43, v43, v43 quad_perm:[2,3,0,1] row_mask:0xf bank_mask:0xf
	s_nop 0
	v_add_f32_dpp v42, v42, v42 row_half_mirror row_mask:0xf bank_mask:0xf
	v_add_f32_dpp v43, v43, v43 row_half_mirror row_mask:0xf bank_mask:0xf
	s_nop 0
	v_add_f32_dpp v42, v42, v42 row_mirror row_mask:0xf bank_mask:0xf
	v_add_f32_dpp v43, v43, v43 row_mirror row_mask:0xf bank_mask:0xf
	s_nop 0
	v_add_f32_dpp v42, v42, v42 row_bcast:15 row_mask:0xa bank_mask:0xf
	v_add_f32_dpp v43, v43, v43 row_bcast:15 row_mask:0xa bank_mask:0xf
	s_nop 0
	v_add_f32_dpp v42, v42, v42 row_bcast:31 row_mask:0xc bank_mask:0xf
	v_add_f32_dpp v43, v43, v43 row_bcast:31 row_mask:0xc bank_mask:0xf
	s_nop 0
	s_mov_b32 s4, 0
	s_brev_b32 s5, 1
	s_mov_b64 exec, s[4:5]
	v_lshlrev_b32_e32 v1, 3, v62
	ds_write_b64 v1, v[42:43] offset:8192
	s_mov_b64 exec, -1
